# baseline (speedup 1.0000x reference)
.LBB1_50:
	s_or_saveexec_b64 s[38:39], s[0:1]
	s_add_i32 s41, s67, s40
	s_mul_i32 s40, s69, 0x62
	s_xor_b64 exec, exec, s[38:39]
	s_cbranch_execz .LBB1_57
	v_mov_b32_e32 v35, 0
	ds_read_b32 v54, v35 offset:27144
	s_cmp_eq_u32 s68, 1
	s_cselect_b64 vcc, -1, 0
	v_sub_u32_e32 v46, v46, v31
	v_lshlrev_b32_e32 v55, 2, v0
	s_waitcnt lgkmcnt(0)
	v_cndmask_b32_e32 v56, 0, v54, vcc
	v_add_u32_e32 v46, v46, v56
	ds_write_b32 v55, v34 offset:27664
	v_add_u32_e32 v34, 0x6800, v55
	s_movk_i32 s0, 0x62
	ds_write2_b32 v34, v46, v31 offset1:132
	v_add_u32_e32 v34, s40, v0
	v_cmp_gt_u32_e32 vcc, s0, v0
	s_mov_b32 s0, 0x186a0
	v_cmp_gt_u32_e64 s[0:1], s0, v34
	s_and_b64 s[42:43], vcc, s[0:1]
	s_and_saveexec_b64 s[0:1], s[42:43]
	s_cbranch_execz .LBB1_53
	v_lshl_add_u64 v[34:35], v[34:35], 2, s[52:53]
	v_add_u32_e32 v31, s41, v46
	global_store_dword v[34:35], v31, off nt
.LBB1_53:
	s_or_b64 exec, exec, s[0:1]
	v_cmp_eq_u32_e32 vcc, 0, v0
	s_and_saveexec_b64 s[0:1], vcc
	s_cbranch_execz .LBB1_56
	v_mov_b32_e32 v31, 0
	ds_read_b32 v34, v31 offset:27148
	s_cmpk_lg_i32 s69, 0x3fc
	s_waitcnt lgkmcnt(0)
	v_add_u32_e32 v34, v34, v54
	ds_write_b32 v31, v34 offset:27136
	s_cbranch_scc1 .LBB1_56
	v_mov_b32_e32 v31, 0x61000
	v_mov_b32_e32 v34, 0xf4240
	global_store_dword v31, v34, s[52:53] offset:2688 nt

.LBB1_57:
	s_or_b64 exec, exec, s[38:39]
	s_waitcnt vmcnt(5)
	v_mov_b32_e32 v18, 0
	s_waitcnt lgkmcnt(0)
	s_barrier
	ds_read_b32 v46, v18 offset:27136
	s_movk_i32 s0, 0x801
	s_waitcnt lgkmcnt(0)
	v_cmp_gt_i32_e32 vcc, s0, v46
	s_mov_b64 s[0:1], -1
	s_cbranch_vccnz .LBB1_94
	s_and_saveexec_b64 s[0:1], s[30:31]
	s_cbranch_execz .LBB1_75
	s_waitcnt vmcnt(0)
	v_ashrrev_i32_e32 v18, 17, v14
	v_lshlrev_b32_e32 v18, 2, v18
	ds_read_b32 v18, v18 offset:26624
	v_and_b32_e32 v20, 0x1ffff, v14
	s_waitcnt lgkmcnt(0)
	v_add3_u32 v18, v18, s41, v53
	v_ashrrev_i32_e32 v19, 31, v18
	v_lshl_add_u64 v[18:19], v[18:19], 2, s[54:55]
	global_store_dword v[18:19], v20, off nt
	s_or_b64 exec, exec, s[0:1]
	s_and_saveexec_b64 s[0:1], s[36:37]
	s_cbranch_execnz .LBB1_76

.LBB1_61:
	s_waitcnt vmcnt(0)
	v_ashrrev_i32_e32 v18, 17, v16
	v_lshlrev_b32_e32 v18, 2, v18
	ds_read_b32 v18, v18 offset:26624
	v_and_b32_e32 v20, 0x1ffff, v16
	s_waitcnt lgkmcnt(0)
	v_add3_u32 v18, v18, s41, v37
	v_ashrrev_i32_e32 v19, 31, v18
	v_lshl_add_u64 v[18:19], v[18:19], 2, s[54:55]
	global_store_dword v[18:19], v20, off nt
	s_or_b64 exec, exec, s[0:1]
	s_and_saveexec_b64 s[0:1], s[4:5]
	s_cbranch_execnz .LBB1_78

.LBB1_63:
	s_waitcnt vmcnt(1)
	v_ashrrev_i32_e32 v18, 17, v10
	v_lshlrev_b32_e32 v18, 2, v18
	ds_read_b32 v18, v18 offset:26624
	v_and_b32_e32 v20, 0x1ffff, v10
	s_waitcnt lgkmcnt(0)
	v_add3_u32 v18, v18, s41, v39
	v_ashrrev_i32_e32 v19, 31, v18
	v_lshl_add_u64 v[18:19], v[18:19], 2, s[54:55]
	global_store_dword v[18:19], v20, off nt
	s_or_b64 exec, exec, s[0:1]
	s_and_saveexec_b64 s[0:1], s[8:9]
	s_cbranch_execnz .LBB1_80

.LBB1_65:
	s_waitcnt vmcnt(1)
	v_ashrrev_i32_e32 v18, 17, v12
	v_lshlrev_b32_e32 v18, 2, v18
	ds_read_b32 v18, v18 offset:26624
	v_and_b32_e32 v20, 0x1ffff, v12
	s_waitcnt lgkmcnt(0)
	v_add3_u32 v18, v18, s41, v41
	v_ashrrev_i32_e32 v19, 31, v18
	v_lshl_add_u64 v[18:19], v[18:19], 2, s[54:55]
	global_store_dword v[18:19], v20, off nt
	s_or_b64 exec, exec, s[0:1]
	s_and_saveexec_b64 s[0:1], s[12:13]
	s_cbranch_execnz .LBB1_82

.LBB1_67:
	s_waitcnt vmcnt(2)
	v_ashrrev_i32_e32 v18, 17, v6
	v_lshlrev_b32_e32 v18, 2, v18
	ds_read_b32 v18, v18 offset:26624
	v_and_b32_e32 v20, 0x1ffff, v6
	s_waitcnt lgkmcnt(0)
	v_add3_u32 v18, v18, s41, v43
	v_ashrrev_i32_e32 v19, 31, v18
	v_lshl_add_u64 v[18:19], v[18:19], 2, s[54:55]
	global_store_dword v[18:19], v20, off nt
	s_or_b64 exec, exec, s[0:1]
	s_and_saveexec_b64 s[0:1], s[16:17]
	s_cbranch_execnz .LBB1_84

.LBB1_69:
	s_waitcnt vmcnt(2)
	v_ashrrev_i32_e32 v18, 17, v8
	v_lshlrev_b32_e32 v18, 2, v18
	ds_read_b32 v18, v18 offset:26624
	v_and_b32_e32 v20, 0x1ffff, v8
	s_waitcnt lgkmcnt(0)
	v_add3_u32 v18, v18, s41, v45
	v_ashrrev_i32_e32 v19, 31, v18
	v_lshl_add_u64 v[18:19], v[18:19], 2, s[54:55]
	global_store_dword v[18:19], v20, off nt
	s_or_b64 exec, exec, s[0:1]
	s_and_saveexec_b64 s[0:1], s[20:21]
	s_cbranch_execnz .LBB1_86

.LBB1_71:
	s_waitcnt vmcnt(3)
	v_ashrrev_i32_e32 v18, 17, v2
	v_lshlrev_b32_e32 v18, 2, v18
	ds_read_b32 v18, v18 offset:26624
	v_and_b32_e32 v20, 0x1ffff, v2
	s_waitcnt lgkmcnt(0)
	v_add3_u32 v18, v18, s41, v49
	v_ashrrev_i32_e32 v19, 31, v18
	v_lshl_add_u64 v[18:19], v[18:19], 2, s[54:55]
	global_store_dword v[18:19], v20, off nt
	s_or_b64 exec, exec, s[0:1]
	s_and_saveexec_b64 s[0:1], s[24:25]
	s_cbranch_execnz .LBB1_88

.LBB1_73:
	s_waitcnt vmcnt(3)
	v_ashrrev_i32_e32 v18, 17, v4
	v_lshlrev_b32_e32 v18, 2, v18
	ds_read_b32 v18, v18 offset:26624
	v_and_b32_e32 v20, 0x1ffff, v4
	s_waitcnt lgkmcnt(0)
	v_add3_u32 v18, v18, s41, v51
	v_ashrrev_i32_e32 v19, 31, v18
	v_lshl_add_u64 v[18:19], v[18:19], 2, s[54:55]
	global_store_dword v[18:19], v20, off nt
	s_or_b64 exec, exec, s[0:1]
	s_and_saveexec_b64 s[0:1], s[28:29]
	s_cbranch_execnz .LBB1_90

.LBB1_76:
	s_waitcnt vmcnt(0)
	v_ashrrev_i32_e32 v18, 17, v15
	v_lshlrev_b32_e32 v18, 2, v18
	ds_read_b32 v18, v18 offset:26624
	v_and_b32_e32 v20, 0x1ffff, v15
	s_waitcnt lgkmcnt(0)
	v_add3_u32 v18, v18, s41, v36
	v_ashrrev_i32_e32 v19, 31, v18
	v_lshl_add_u64 v[18:19], v[18:19], 2, s[54:55]
	global_store_dword v[18:19], v20, off nt
	s_or_b64 exec, exec, s[0:1]
	s_and_saveexec_b64 s[0:1], s[2:3]
	s_cbranch_execnz .LBB1_61

.LBB1_78:
	s_waitcnt vmcnt(0)
	v_ashrrev_i32_e32 v18, 17, v17
	v_lshlrev_b32_e32 v18, 2, v18
	ds_read_b32 v18, v18 offset:26624
	v_and_b32_e32 v20, 0x1ffff, v17
	s_waitcnt lgkmcnt(0)
	v_add3_u32 v18, v18, s41, v38
	v_ashrrev_i32_e32 v19, 31, v18
	v_lshl_add_u64 v[18:19], v[18:19], 2, s[54:55]
	global_store_dword v[18:19], v20, off nt
	s_or_b64 exec, exec, s[0:1]
	s_and_saveexec_b64 s[0:1], s[6:7]
	s_cbranch_execnz .LBB1_63

.LBB1_80:
	s_waitcnt vmcnt(1)
	v_ashrrev_i32_e32 v18, 17, v11
	v_lshlrev_b32_e32 v18, 2, v18
	ds_read_b32 v18, v18 offset:26624
	v_and_b32_e32 v20, 0x1ffff, v11
	s_waitcnt lgkmcnt(0)
	v_add3_u32 v18, v18, s41, v40
	v_ashrrev_i32_e32 v19, 31, v18
	v_lshl_add_u64 v[18:19], v[18:19], 2, s[54:55]
	global_store_dword v[18:19], v20, off nt
	s_or_b64 exec, exec, s[0:1]
	s_and_saveexec_b64 s[0:1], s[10:11]
	s_cbranch_execnz .LBB1_65

.LBB1_82:
	s_waitcnt vmcnt(1)
	v_ashrrev_i32_e32 v18, 17, v13
	v_lshlrev_b32_e32 v18, 2, v18
	ds_read_b32 v18, v18 offset:26624
	v_and_b32_e32 v20, 0x1ffff, v13
	s_waitcnt lgkmcnt(0)
	v_add3_u32 v18, v18, s41, v42
	v_ashrrev_i32_e32 v19, 31, v18
	v_lshl_add_u64 v[18:19], v[18:19], 2, s[54:55]
	global_store_dword v[18:19], v20, off nt
	s_or_b64 exec, exec, s[0:1]
	s_and_saveexec_b64 s[0:1], s[14:15]
	s_cbranch_execnz .LBB1_67

.LBB1_84:
	s_waitcnt vmcnt(2)
	v_ashrrev_i32_e32 v18, 17, v7
	v_lshlrev_b32_e32 v18, 2, v18
	ds_read_b32 v18, v18 offset:26624
	v_and_b32_e32 v20, 0x1ffff, v7
	s_waitcnt lgkmcnt(0)
	v_add3_u32 v18, v18, s41, v44
	v_ashrrev_i32_e32 v19, 31, v18
	v_lshl_add_u64 v[18:19], v[18:19], 2, s[54:55]
	global_store_dword v[18:19], v20, off nt
	s_or_b64 exec, exec, s[0:1]
	s_and_saveexec_b64 s[0:1], s[18:19]
	s_cbranch_execnz .LBB1_69

.LBB1_86:
	s_waitcnt vmcnt(2)
	v_ashrrev_i32_e32 v18, 17, v9
	v_lshlrev_b32_e32 v18, 2, v18
	ds_read_b32 v18, v18 offset:26624
	v_and_b32_e32 v20, 0x1ffff, v9
	s_waitcnt lgkmcnt(0)
	v_add3_u32 v18, v18, s41, v47
	v_ashrrev_i32_e32 v19, 31, v18
	v_lshl_add_u64 v[18:19], v[18:19], 2, s[54:55]
	global_store_dword v[18:19], v20, off nt
	s_or_b64 exec, exec, s[0:1]
	s_and_saveexec_b64 s[0:1], s[22:23]
	s_cbranch_execnz .LBB1_71

.LBB1_88:
	s_waitcnt vmcnt(3)
	v_ashrrev_i32_e32 v18, 17, v3
	v_lshlrev_b32_e32 v18, 2, v18
	ds_read_b32 v18, v18 offset:26624
	v_and_b32_e32 v20, 0x1ffff, v3
	s_waitcnt lgkmcnt(0)
	v_add3_u32 v18, v18, s41, v50
	v_ashrrev_i32_e32 v19, 31, v18
	v_lshl_add_u64 v[18:19], v[18:19], 2, s[54:55]
	global_store_dword v[18:19], v20, off nt
	s_or_b64 exec, exec, s[0:1]
	s_and_saveexec_b64 s[0:1], s[26:27]
	s_cbranch_execnz .LBB1_73

.LBB1_90:
	s_waitcnt vmcnt(3)
	v_ashrrev_i32_e32 v18, 17, v5
	v_lshlrev_b32_e32 v18, 2, v18
	ds_read_b32 v18, v18 offset:26624
	v_and_b32_e32 v20, 0x1ffff, v5
	s_waitcnt lgkmcnt(0)
	v_add3_u32 v18, v18, s41, v52
	v_ashrrev_i32_e32 v19, 31, v18
	v_lshl_add_u64 v[18:19], v[18:19], 2, s[54:55]
	global_store_dword v[18:19], v20, off nt
	s_or_b64 exec, exec, s[0:1]
	s_and_saveexec_b64 s[0:1], s[34:35]
	s_cbranch_execz .LBB1_93

.LBB1_92:
	global_load_dword v22, v[18:19], off
	v_add_u32_e32 v21, 1, v21
	v_cmp_ge_i32_e32 vcc, v21, v33
	v_lshl_add_u64 v[18:19], v[18:19], 0, 4
	s_or_b64 s[38:39], vcc, s[38:39]
	s_waitcnt vmcnt(0)
	v_ashrrev_i32_e32 v23, 17, v22
	v_lshlrev_b32_e32 v23, 2, v23
	ds_add_rtn_u32 v24, v23, v20 offset:27664
	ds_read_b32 v23, v23 offset:26624
	v_and_b32_e32 v25, 0x1ffff, v22
	s_waitcnt lgkmcnt(0)
	v_add3_u32 v22, v24, s41, v23
	v_ashrrev_i32_e32 v23, 31, v22
	v_lshl_add_u64 v[22:23], v[22:23], 2, s[54:55]
	global_store_dword v[22:23], v25, off nt
	s_andn2_b64 exec, exec, s[38:39]
	s_cbranch_execnz .LBB1_92

.LBB1_135:
	ds_read2st64_b32 v[4:5], v49 offset1:8
	v_add_u32_e32 v10, s41, v2
	ds_read2st64_b32 v[6:7], v49 offset0:16 offset1:24
	v_add_u32_e32 v47, -8, v47
	v_add_u32_e32 v8, s41, v3
	v_add_u32_e32 v16, s13, v2
	v_add_u32_e32 v14, s14, v3
	v_add_u32_e32 v22, s15, v2
	v_add_u32_e32 v20, s16, v3
	v_add_u32_e32 v28, s17, v2
	v_add_u32_e32 v26, s18, v3
	v_add_u32_e32 v34, s19, v2
	v_add_u32_e32 v32, s20, v3
	v_add_u32_e32 v40, s21, v2
	v_add_u32_e32 v38, s22, v3
	v_add_u32_e32 v52, s23, v2
	v_add_u32_e32 v54, s24, v3
	v_add_u32_e32 v56, s25, v2
	v_add_u32_e32 v58, s26, v3
	s_add_i32 s12, s12, 16
	v_ashrrev_i32_e32 v11, 31, v10
	v_cmp_eq_u32_e32 vcc, 0, v47
	ds_read2st64_b32 v[12:13], v49 offset0:32 offset1:40
	ds_read2st64_b32 v[18:19], v49 offset0:48 offset1:56
	ds_read2st64_b32 v[24:25], v49 offset0:64 offset1:72
	ds_read2st64_b32 v[30:31], v49 offset0:80 offset1:88
	ds_read2st64_b32 v[36:37], v49 offset0:96 offset1:104
	ds_read2st64_b32 v[42:43], v49 offset0:112 offset1:120
	v_add_u32_e32 v3, 0x2000, v3
	v_add_u32_e32 v2, 0x2000, v2
	v_add_u32_e32 v49, 0x8000, v49
	v_ashrrev_i32_e32 v9, 31, v8
	v_ashrrev_i32_e32 v15, 31, v14
	v_ashrrev_i32_e32 v17, 31, v16
	v_ashrrev_i32_e32 v21, 31, v20
	v_ashrrev_i32_e32 v23, 31, v22
	v_ashrrev_i32_e32 v27, 31, v26
	v_ashrrev_i32_e32 v29, 31, v28
	v_ashrrev_i32_e32 v33, 31, v32
	v_ashrrev_i32_e32 v35, 31, v34
	v_ashrrev_i32_e32 v39, 31, v38
	v_ashrrev_i32_e32 v41, 31, v40
	v_ashrrev_i32_e32 v55, 31, v54
	v_ashrrev_i32_e32 v53, 31, v52
	v_ashrrev_i32_e32 v59, 31, v58
	v_ashrrev_i32_e32 v57, 31, v56
	v_mov_b32_e32 v50, s12
	v_lshl_add_u64 v[10:11], v[10:11], 2, s[54:55]
	s_or_b64 s[10:11], vcc, s[10:11]
	v_lshl_add_u64 v[8:9], v[8:9], 2, s[54:55]
	v_lshl_add_u64 v[16:17], v[16:17], 2, s[54:55]
	v_lshl_add_u64 v[14:15], v[14:15], 2, s[54:55]
	v_lshl_add_u64 v[22:23], v[22:23], 2, s[54:55]
	v_lshl_add_u64 v[20:21], v[20:21], 2, s[54:55]
	v_lshl_add_u64 v[28:29], v[28:29], 2, s[54:55]
	v_lshl_add_u64 v[26:27], v[26:27], 2, s[54:55]
	v_lshl_add_u64 v[34:35], v[34:35], 2, s[54:55]
	v_lshl_add_u64 v[32:33], v[32:33], 2, s[54:55]
	v_lshl_add_u64 v[40:41], v[40:41], 2, s[54:55]
	v_lshl_add_u64 v[38:39], v[38:39], 2, s[54:55]
	v_lshl_add_u64 v[52:53], v[52:53], 2, s[54:55]
	v_lshl_add_u64 v[54:55], v[54:55], 2, s[54:55]
	v_lshl_add_u64 v[56:57], v[56:57], 2, s[54:55]
	v_lshl_add_u64 v[58:59], v[58:59], 2, s[54:55]
	s_waitcnt lgkmcnt(7)
	global_store_dword v[10:11], v4, off nt
	global_store_dword v[8:9], v5, off nt
	s_waitcnt lgkmcnt(6)
	global_store_dword v[16:17], v6, off nt
	global_store_dword v[14:15], v7, off nt
	s_waitcnt lgkmcnt(5)
	global_store_dword v[22:23], v12, off nt
	global_store_dword v[20:21], v13, off nt
	s_waitcnt lgkmcnt(4)
	global_store_dword v[28:29], v18, off nt
	global_store_dword v[26:27], v19, off nt
	s_waitcnt lgkmcnt(3)
	global_store_dword v[34:35], v24, off nt
	global_store_dword v[32:33], v25, off nt
	s_waitcnt lgkmcnt(2)
	global_store_dword v[40:41], v30, off nt
	global_store_dword v[38:39], v31, off nt
	s_waitcnt lgkmcnt(1)
	global_store_dword v[52:53], v36, off nt
	global_store_dword v[54:55], v37, off nt
	s_waitcnt lgkmcnt(0)
	global_store_dword v[56:57], v42, off nt
	global_store_dword v[58:59], v43, off nt
	s_andn2_b64 exec, exec, s[10:11]
	s_cbranch_execnz .LBB1_135
	s_or_b64 exec, exec, s[10:11]

.LBB1_139:
	ds_read2st64_b32 v[6:7], v4 offset1:8
	v_add_u32_e32 v8, s41, v2
	v_add_u32_e32 v1, -1, v1
	v_add_u32_e32 v10, s41, v3
	v_ashrrev_i32_e32 v9, 31, v8
	v_cmp_eq_u32_e32 vcc, 0, v1
	v_add_u32_e32 v3, 0x400, v3
	v_add_u32_e32 v2, 0x400, v2
	v_add_u32_e32 v4, 0x1000, v4
	v_ashrrev_i32_e32 v11, 31, v10
	v_lshl_add_u64 v[8:9], v[8:9], 2, s[54:55]
	s_or_b64 s[10:11], vcc, s[10:11]
	v_lshl_add_u64 v[10:11], v[10:11], 2, s[54:55]
	s_waitcnt lgkmcnt(0)
	global_store_dword v[8:9], v6, off nt
	global_store_dword v[10:11], v7, off nt
	s_andn2_b64 exec, exec, s[10:11]
	s_cbranch_execnz .LBB1_139

.LBB1_144:
	ds_read_b32 v5, v4
	v_add_u32_e32 v1, 0x200, v1
	v_ashrrev_i32_e32 v3, 31, v2
	v_cmp_ge_i32_e32 vcc, v1, v46
	v_add_u32_e32 v4, 0x800, v4
	v_lshl_add_u64 v[6:7], v[2:3], 2, s[54:55]
	v_add_u32_e32 v2, 0x200, v2
	s_or_b64 s[2:3], vcc, s[2:3]
	s_waitcnt lgkmcnt(0)
	global_store_dword v[6:7], v5, off nt
	s_andn2_b64 exec, exec, s[2:3]
	s_cbranch_execnz .LBB1_144

.LBB1_158:
	s_or_b64 exec, exec, s[8:9]
	v_and_b32_e32 v9, 15, v0
	s_add_i32 s0, s16, s40
	v_cmp_gt_u32_e32 vcc, 14, v9
	v_add_u32_e32 v0, s0, v9
	s_and_b64 s[0:1], vcc, s[2:3]
	v_add_u32_e32 v1, s16, v9
	s_movk_i32 s2, 0x62
	v_cmp_gt_u32_e32 vcc, s2, v1
	s_mov_b32 s2, 0x186a0
	s_and_b64 s[0:1], s[0:1], vcc
	v_cmp_gt_u32_e32 vcc, s2, v0
	s_and_b64 s[0:1], s[0:1], vcc
	v_mov_b32_e32 v29, 0
	v_cndmask_b32_e64 v28, 0, v0, s[0:1]
	v_lshlrev_b64 v[0:1], 7, v[28:29]
	v_lshl_add_u64 v[0:1], s[56:57], 0, v[0:1]
	v_and_b32_e32 v20, -16, v48
	v_mov_b32_e32 v21, v29
	v_lshl_add_u64 v[0:1], v[0:1], 0, v[20:21]
	global_load_dwordx4 v[4:7], v[0:1], off
	s_nop 0
	global_load_dwordx4 v[0:3], v[0:1], off offset:64
	v_cvt_f32_i32_e32 v8, v51
	s_waitcnt vmcnt(3)
	v_lshrrev_b32_e32 v12, 4, v48
	v_lshlrev_b32_e32 v46, 4, v48
	v_max_f32_e32 v8, 1.0, v8
	v_div_scale_f32 v10, s[2:3], v8, v8, 1.0
	v_rcp_f32_e32 v11, v10
	s_nop 0
	v_fma_f32 v13, -v10, v11, 1.0
	v_fmac_f32_e32 v11, v13, v11
	v_div_scale_f32 v13, vcc, 1.0, v8, 1.0
	s_waitcnt vmcnt(2)
	v_mul_f32_e32 v14, v13, v11
	v_fma_f32 v15, -v10, v14, v13
	v_fmac_f32_e32 v14, v15, v11
	v_fma_f32 v10, -v10, v14, v13
	v_div_fmas_f32 v10, v10, v11, v14
	v_div_fixup_f32 v8, v10, v8, 1.0
	v_pk_mul_f32 v[10:11], v[8:9], v[44:45] op_sel_hi:[0,1]
	v_cvt_pk_f16_f32 v15, v10, v11
	v_pk_mul_f32 v[10:11], v[8:9], v[42:43] op_sel_hi:[0,1]
	v_cvt_pk_f16_f32 v16, v10, v11
	v_pk_mul_f32 v[10:11], v[8:9], v[40:41] op_sel_hi:[0,1]
	v_cvt_pk_f16_f32 v17, v10, v11
	v_pk_mul_f32 v[10:11], v[8:9], v[38:39] op_sel_hi:[0,1]
	v_cvt_pk_f16_f32 v18, v10, v11
	v_pk_mul_f32 v[10:11], v[8:9], v[36:37] op_sel_hi:[0,1]
	v_fma_mixlo_f16 v13, v8, v53, 0
	v_cvt_pk_f16_f32 v10, v10, v11
	v_pack_b32_f16 v13, v13, v15
	v_alignbit_b32 v15, v17, v15, 16
	v_alignbit_b32 v17, v10, v17, 16
	v_lshrrev_b32_e32 v19, 16, v10
	v_pk_mul_f32 v[10:11], v[8:9], v[34:35] op_sel_hi:[0,1]
	v_fma_mixlo_f16 v14, v8, v54, 0
	v_cvt_pk_f16_f32 v10, v10, v11
	v_pack_b32_f16 v14, v14, v16
	v_alignbit_b32 v16, v18, v16, 16
	v_alignbit_b32 v11, v10, v18, 16
	v_lshrrev_b32_e32 v18, 16, v10
	v_fma_mixhi_f16 v19, v8, v52, 0
	v_fma_mixhi_f16 v18, v8, v50, 0
	v_lshlrev_b32_e32 v8, 2, v9
	v_or3_b32 v8, v49, v8, v12
	v_lshlrev_b32_e32 v21, 2, v8
	ds_bpermute_b32 v12, v21, v13
	ds_bpermute_b32 v8, v21, v14
	ds_bpermute_b32 v13, v21, v15
	ds_bpermute_b32 v9, v21, v16
	ds_bpermute_b32 v14, v21, v17
	ds_bpermute_b32 v10, v21, v11
	ds_bpermute_b32 v15, v21, v19
	ds_bpermute_b32 v11, v21, v18
	global_load_dwordx4 v[16:19], v20, s[48:49]
	ds_read_b128 v[22:25], v46
	ds_read_b128 v[30:33], v46 offset:1024
	s_waitcnt vmcnt(0) lgkmcnt(1)
	v_mfma_f32_16x16x32_f16 v[16:19], v[22:25], v[12:15], v[16:19]
	ds_read_b128 v[22:25], v46 offset:2048
	s_waitcnt lgkmcnt(1)
	v_mfma_f32_16x16x32_f16 v[16:19], v[30:33], v[8:11], v[16:19]
	ds_read_b128 v[30:33], v46 offset:3072
	s_waitcnt lgkmcnt(1)
	v_mfma_f32_16x16x32_f16 v[16:19], v[22:25], v[4:7], v[16:19]
	s_waitcnt lgkmcnt(0)
	v_mfma_f32_16x16x32_f16 v[30:33], v[30:33], v[0:3], v[16:19]
	s_nop 5
	global_load_dwordx4 v[16:19], v20, s[48:49] offset:64
	ds_read_b128 v[22:25], v46 offset:4096
	ds_read_b128 v[34:37], v46 offset:5120
	s_waitcnt vmcnt(0) lgkmcnt(1)
	v_mfma_f32_16x16x32_f16 v[16:19], v[22:25], v[12:15], v[16:19]
	ds_read_b128 v[22:25], v46 offset:6144
	s_waitcnt lgkmcnt(1)
	v_mfma_f32_16x16x32_f16 v[16:19], v[34:37], v[8:11], v[16:19]
	ds_read_b128 v[34:37], v46 offset:7168
	s_waitcnt lgkmcnt(1)
	v_mfma_f32_16x16x32_f16 v[16:19], v[22:25], v[4:7], v[16:19]
	s_waitcnt lgkmcnt(0)
	v_mfma_f32_16x16x32_f16 v[34:37], v[34:37], v[0:3], v[16:19]
	s_nop 5
	global_load_dwordx4 v[16:19], v20, s[48:49] offset:128
	ds_read_b128 v[22:25], v46 offset:8192
	ds_read_b128 v[38:41], v46 offset:9216
	s_waitcnt vmcnt(0) lgkmcnt(1)
	v_mfma_f32_16x16x32_f16 v[16:19], v[22:25], v[12:15], v[16:19]
	ds_read_b128 v[22:25], v46 offset:10240
	s_waitcnt lgkmcnt(1)
	v_mfma_f32_16x16x32_f16 v[16:19], v[38:41], v[8:11], v[16:19]
	ds_read_b128 v[38:41], v46 offset:11264
	s_waitcnt lgkmcnt(1)
	v_mfma_f32_16x16x32_f16 v[16:19], v[22:25], v[4:7], v[16:19]
	s_waitcnt lgkmcnt(0)
	v_mfma_f32_16x16x32_f16 v[16:19], v[38:41], v[0:3], v[16:19]
	global_load_dwordx4 v[20:23], v20, s[48:49] offset:192
	ds_read_b128 v[24:27], v46 offset:12288
	s_load_dwordx2 s[2:3], s[50:51], 0x0
	v_max_f32_e32 v43, v34, v34
	v_max_f32_e32 v45, v35, v35
	v_max_f32_e32 v47, v36, v36
	v_max_f32_e32 v49, v37, v37
	ds_read_b128 v[34:37], v46 offset:24576
	ds_read_b128 v[38:41], v46 offset:25600
	v_max_f32_e32 v42, v30, v30
	v_max_f32_e32 v44, v31, v31
	v_max_f32_e32 v32, v32, v32
	v_max_f32_e32 v33, v33, v33
	v_max_f32_e32 v42, 0, v42
	v_max_f32_e32 v43, 0, v43
	v_max_f32_e32 v50, 0, v44
	v_max_f32_e32 v44, 0, v45
	v_max_f32_e32 v32, 0, v32
	v_max_f32_e32 v45, 0, v47
	v_max_f32_e32 v33, 0, v33
	v_max_f32_e32 v47, 0, v49
	v_mov_b32_e32 v30, v29
	v_mov_b32_e32 v31, v29
	v_cvt_pk_f16_f32 v45, v45, v47
	v_cvt_pk_f16_f32 v44, v43, v44
	v_cvt_pk_f16_f32 v43, v32, v33
	v_cvt_pk_f16_f32 v42, v42, v50
	s_waitcnt lgkmcnt(0)
	v_mov_b32_e32 v32, s2
	v_mov_b32_e32 v33, s3
	v_max_f32_e32 v16, v16, v16
	v_max_f32_e32 v17, v17, v17
	v_mfma_f32_16x16x32_f16 v[30:33], v[34:37], v[42:45], v[30:33]
	ds_read_b128 v[34:37], v46 offset:13312
	ds_read_b128 v[42:45], v46 offset:14336
	ds_read_b128 v[50:53], v46 offset:15360
	v_max_f32_e32 v18, v18, v18
	v_cmp_gt_u32_e32 vcc, 16, v48
	s_and_b64 s[0:1], s[0:1], vcc
	s_waitcnt vmcnt(0)
	v_mfma_f32_16x16x32_f16 v[12:15], v[24:27], v[12:15], v[20:23]
	s_waitcnt lgkmcnt(2)
	v_mfma_f32_16x16x32_f16 v[8:11], v[34:37], v[8:11], v[12:15]
	s_waitcnt lgkmcnt(1)
	v_mfma_f32_16x16x32_f16 v[4:7], v[42:45], v[4:7], v[8:11]
	s_nop 3
	v_max_f32_e32 v12, v19, v19
	v_max_f32_e32 v13, 0, v16
	v_max_f32_e32 v14, 0, v17
	s_waitcnt lgkmcnt(0)
	v_mfma_f32_16x16x32_f16 v[0:3], v[50:53], v[0:3], v[4:7]
	v_max_f32_e32 v8, 0, v18
	v_max_f32_e32 v9, 0, v12
	v_cvt_pk_f16_f32 v9, v8, v9
	v_cvt_pk_f16_f32 v8, v13, v14
	s_nop 3
	v_max_f32_e32 v0, v0, v0
	v_max_f32_e32 v1, v1, v1
	v_max_f32_e32 v2, v2, v2
	v_max_f32_e32 v3, v3, v3
	v_max_f32_e32 v0, 0, v0
	v_max_f32_e32 v1, 0, v1
	v_max_f32_e32 v2, 0, v2
	v_max_f32_e32 v3, 0, v3
	v_cvt_pk_f16_f32 v11, v2, v3
	v_cvt_pk_f16_f32 v10, v0, v1
	s_nop 1
	v_mfma_f32_16x16x32_f16 v[0:3], v[38:41], v[8:11], v[30:33]
	s_and_saveexec_b64 s[2:3], s[0:1]
	s_cbranch_execz .LBB1_160
	v_lshlrev_b64 v[4:5], 3, v[28:29]
	v_lshl_add_u64 v[6:7], s[44:45], 0, v[4:5]
	s_nop 3
	global_store_dwordx2 v[6:7], v[0:1], off nt
	v_lshl_add_u64 v[0:1], s[46:47], 0, v[4:5]
	global_store_dwordx2 v[0:1], v[2:3], off nt
